# speedup vs baseline: 1.0106x; 1.0097x over previous
.LBB1_6:
	v_min_f32_e64 v34, |v66|, |v82|
	s_nop 0
	v_min3_f32 v34, v34, |v67|, |v83|
	v_min3_f32 v34, v34, |v68|, |v84|
	v_min3_f32 v34, v34, |v69|, |v85|
	v_min3_f32 v34, v34, |v70|, |v86|
	v_min3_f32 v34, v34, |v71|, |v87|
	v_min3_f32 v34, v34, |v72|, |v88|
	v_min3_f32 v34, v34, |v73|, |v89|
	v_min3_f32 v34, v34, |v74|, |v90|
	v_min3_f32 v34, v34, |v75|, |v91|
	v_min3_f32 v34, v34, |v76|, |v92|
	v_min3_f32 v34, v34, |v77|, |v93|
	v_min3_f32 v34, v34, |v78|, |v94|
	v_min3_f32 v34, v34, |v79|, |v95|
	v_min3_f32 v34, v34, |v80|, |v96|
	v_min3_f32 v34, v34, |v81|, |v97|
	v_cmp_eq_f32_e32 vcc, 0, v34
	s_cbranch_vccnz .LBB1_28
.LBB1_7:
.LBB1_8:
	v_max_f32_e32 v50, v66, v67
	v_max3_f32 v51, v68, v69, v83
	v_max3_f32 v50, v50, v82, v84
	v_max3_f32 v50, v50, v85, v70
	v_max3_f32 v51, v51, v72, v73
	v_max3_f32 v50, v50, v71, v86
	v_max3_f32 v51, v51, v88, v89
	v_max3_f32 v50, v50, v87, v74
	v_max3_f32 v51, v51, v76, v77
	v_max3_f32 v50, v50, v75, v90
	v_max3_f32 v51, v51, v92, v93
	v_max3_f32 v50, v50, v91, v78
	v_max3_f32 v51, v51, v80, v81
	v_max3_f32 v50, v50, v79, v94
	v_max3_f32 v51, v51, v96, v97
	v_max3_f32 v50, v50, v95, v51
	v_mov_b32_e32 v51, v50
	s_nop 1
	v_permlane32_swap_b32_e32 v50, v51
	v_max_f32_e32 v50, v50, v51
	v_cmp_lt_f32_e32 vcc, s47, v50
	s_cmp_lg_u64 vcc, 0
	v_add_f32_e32 v181, v218, v160
	s_cselect_b64 s[2:3], -1, 0
	s_cbranch_vccnz .LBB1_21

.LBB1_13:
	v_min_f32_e64 v82, |v50|, |v34|
	s_nop 0
	v_min3_f32 v82, v82, |v51|, |v35|
	v_min3_f32 v82, v82, |v52|, |v36|
	v_min3_f32 v82, v82, |v53|, |v37|
	v_min3_f32 v82, v82, |v54|, |v38|
	v_min3_f32 v82, v82, |v55|, |v39|
	v_min3_f32 v82, v82, |v56|, |v40|
	v_min3_f32 v82, v82, |v57|, |v41|
	v_min3_f32 v82, v82, |v58|, |v42|
	v_min3_f32 v82, v82, |v59|, |v43|
	v_min3_f32 v82, v82, |v60|, |v44|
	v_min3_f32 v82, v82, |v61|, |v45|
	v_min3_f32 v82, v82, |v62|, |v46|
	v_min3_f32 v82, v82, |v63|, |v47|
	v_min3_f32 v82, v82, |v64|, |v48|
	v_min3_f32 v82, v82, |v65|, |v49|
	v_cmp_eq_f32_e32 vcc, 0, v82
	s_cbranch_vccnz .LBB1_29
.LBB1_14:
.LBB1_15:
	v_max_f32_e32 v66, v50, v51
	v_max3_f32 v67, v52, v53, v35
	v_max3_f32 v66, v66, v34, v36
	v_max3_f32 v66, v66, v37, v54
	v_max3_f32 v67, v67, v56, v57
	v_max3_f32 v66, v66, v55, v38
	v_max3_f32 v67, v67, v40, v41
	v_max3_f32 v66, v66, v39, v58
	v_max3_f32 v67, v67, v60, v61
	v_max3_f32 v66, v66, v59, v42
	v_max3_f32 v67, v67, v44, v45
	v_max3_f32 v66, v66, v43, v62
	v_max3_f32 v67, v67, v64, v65
	v_max3_f32 v66, v66, v63, v46
	v_max3_f32 v67, v67, v48, v49
	v_max3_f32 v66, v66, v47, v67
	v_mov_b32_e32 v67, v66
	s_nop 1
	v_permlane32_swap_b32_e32 v66, v67
	v_max_f32_e32 v66, v66, v67
	v_cmp_lt_f32_e32 vcc, s47, v66
	s_cmp_lg_u64 vcc, 0
	v_add_f32_e32 v218, v181, v156
	s_cselect_b64 s[30:31], -1, 0
	s_cbranch_vccnz .LBB1_25

.LBB1_30:
	s_nop 0
	s_nop 0
	s_nop 0
	s_nop 0
	s_nop 0
	s_nop 0
	s_nop 0
	s_nop 0
	s_nop 0
	s_nop 0
	s_nop 0
	s_nop 0
	s_add_i32 s24, s46, -4
	s_cmp_ge_u32 s24, s44
	s_cbranch_scc1 .LBB1_39
	s_xor_b64 s[2:3], s[20:21], -1
	s_add_i32 s22, s24, 1
	v_add_u32_e32 v126, s45, v215
	ds_read_b64_tr_b16 v[122:123], v126 offset:49152
	ds_read_b64_tr_b16 v[124:125], v126 offset:49664
	v_add_f32_e32 v70, v50, v51
	v_add_f32_e32 v70, v52, v70
	v_add_f32_e32 v70, v53, v70
	v_add_f32_e32 v70, v54, v70
	v_add_f32_e32 v86, v55, v70
	s_waitcnt lgkmcnt(9)
	v_mfma_f32_32x32x16_f16 v[66:81], v[66:69], v[144:147], 0
	v_cvt_pk_f16_f32 v128, v50, v51
	v_cvt_pk_f16_f32 v129, v52, v53
	s_mov_b32 s23, 0
	ds_read_b64_tr_b16 v[184:185], v126 offset:53248
	ds_read_b64_tr_b16 v[186:187], v126 offset:53760
	v_add_f32_e32 v50, v56, v86
	s_waitcnt lgkmcnt(10)
	v_mfma_f32_32x32x16_f16 v[82:97], v[82:85], v[144:147], 0
	v_add_f32_e32 v50, v57, v50
	v_add_f32_e32 v50, v58, v50
	v_add_f32_e32 v50, v59, v50
	v_cvt_pk_f16_f32 v130, v54, v55
	v_cvt_pk_f16_f32 v131, v56, v57
	s_nop 0
	ds_read_b64_tr_b16 v[176:177], v126 offset:50176
	ds_read_b64_tr_b16 v[178:179], v126 offset:50688
	s_waitcnt lgkmcnt(11)
	v_mfma_f32_32x32x16_f16 v[66:81], v[168:171], v[140:143], v[66:81]
	v_add_f32_e32 v50, v60, v50
	v_add_f32_e32 v50, v61, v50
	v_add_f32_e32 v50, v62, v50
	v_add_f32_e32 v50, v63, v50
	v_cvt_pk_f16_f32 v106, v58, v59
	v_cvt_pk_f16_f32 v107, v60, v61
	s_nop 0
	ds_read_b64_tr_b16 v[118:119], v126 offset:54272
	ds_read_b64_tr_b16 v[120:121], v126 offset:54784
	s_waitcnt lgkmcnt(12)
	v_mfma_f32_32x32x16_f16 v[82:97], v[164:167], v[140:143], v[82:97]
	v_add_f32_e32 v50, v64, v50
	v_add_f32_e32 v50, v65, v50
	v_add_f32_e32 v50, v34, v50
	v_add_f32_e32 v50, v35, v50
	v_cvt_pk_f16_f32 v108, v62, v63
	v_cvt_pk_f16_f32 v109, v64, v65
	s_nop 0
	ds_read_b64_tr_b16 v[114:115], v126 offset:51200
	ds_read_b64_tr_b16 v[116:117], v126 offset:51712
	s_waitcnt lgkmcnt(13)
	v_mfma_f32_32x32x16_f16 v[66:81], v[160:163], v[136:139], v[66:81]
	v_add_f32_e32 v50, v36, v50
	v_add_f32_e32 v50, v37, v50
	v_add_f32_e32 v50, v38, v50
	v_add_f32_e32 v50, v39, v50
	v_cvt_pk_f16_f32 v102, v34, v35
	v_cvt_pk_f16_f32 v103, v36, v37
	s_nop 0
	ds_read_b64_tr_b16 v[110:111], v126 offset:55296
	ds_read_b64_tr_b16 v[112:113], v126 offset:55808
	s_waitcnt lgkmcnt(14)
	v_mfma_f32_32x32x16_f16 v[82:97], v[156:159], v[136:139], v[82:97]
	v_add_f32_e32 v34, v40, v50
	v_add_f32_e32 v34, v41, v34
	v_add_f32_e32 v34, v42, v34
	v_add_f32_e32 v34, v43, v34
	v_cvt_pk_f16_f32 v104, v38, v39
	v_cvt_pk_f16_f32 v105, v40, v41
	s_nop 0
	ds_read_b64_tr_b16 v[172:173], v126 offset:52224
	ds_read_b64_tr_b16 v[174:175], v126 offset:52736
	s_waitcnt lgkmcnt(14)
	v_mfma_f32_32x32x16_f16 v[66:81], v[152:155], v[132:135], v[66:81]
	v_add_f32_e32 v34, v44, v34
	v_add_f32_e32 v34, v45, v34
	v_add_f32_e32 v34, v46, v34
	v_add_f32_e32 v34, v47, v34
	v_cvt_pk_f16_f32 v98, v42, v43
	v_cvt_pk_f16_f32 v99, v44, v45
	s_nop 0
	ds_read_b64_tr_b16 v[180:181], v126 offset:56320
	ds_read_b64_tr_b16 v[182:183], v126 offset:56832
	v_mfma_f32_32x32x16_f16 v[82:97], v[148:151], v[132:135], v[82:97]
	v_add_f32_e32 v34, v48, v34
	v_add_f32_e32 v34, v49, v34
	v_add_f32_e32 v126, 0, v34
	v_cvt_pk_f16_f32 v100, v46, v47
	v_cvt_pk_f16_f32 v101, v48, v49
	s_nop 0
	s_add_i32 s24, s33, s24
	s_add_i32 s24, s24, -13
	s_min_i32 s24, s24, s33
	s_ashr_i32 s25, s24, 31
	s_lshl_b64 s[24:25], s[24:25], 18
	v_lshl_add_u64 v[34:35], v[194:195], 0, s[24:25]
	s_add_i32 s26, s43, s41
	s_mov_b32 s24, m0
	s_mov_b32 m0, s26
	s_nop 0
	global_load_lds_dwordx4 v[34:35], off
	s_mov_b32 m0, s24
	s_mov_b64 s[24:25], 0x20000
	v_lshl_add_u64 v[34:35], v[34:35], 0, s[24:25]
	s_addk_i32 s26, 0x2000
	s_mov_b32 s27, m0
	s_mov_b32 m0, s26
	s_nop 0
	global_load_lds_dwordx4 v[34:35], off
	s_mov_b32 m0, s27
	s_lshl_b64 s[22:23], s[22:23], 18
	v_lshl_add_u64 v[34:35], v[196:197], 0, s[22:23]
	s_add_i32 s22, s30, s40
	s_mov_b32 s23, m0
	s_mov_b32 m0, s22
	s_nop 0
	global_load_lds_dwordx4 v[34:35], off
	s_mov_b32 m0, s23
	v_lshl_add_u64 v[34:35], v[34:35], 0, s[24:25]
	s_addk_i32 s22, 0x2000
	s_andn2_b64 vcc, exec, s[2:3]
	s_mov_b32 s2, m0
	s_mov_b32 m0, s22
	s_nop 0
	global_load_lds_dwordx4 v[34:35], off
	s_mov_b32 m0, s2
	s_cbranch_vccz .LBB1_120
